# speedup vs baseline: 1.0247x; 1.0092x over previous
.LBB1_33:
	s_cmp_gt_u32 s43, 22
	s_cselect_b64 s[38:39], -1, 0
	s_xor_b32 s8, s12, 1
	v_cmp_eq_u32_e64 s[4:5], -1, v190
	v_mov_b32_e32 v159, v142
	v_mov_b32_e32 v160, v140
	s_mulk_i32 s8, 0x4200
	s_mov_b64 s[52:53], s[6:7]
	s_mov_b32 s45, 0
	s_barrier
	s_cmp_lg_u64 s[10:11], 0
	s_cbranch_scc1 .Lq_noearly
	global_load_dwordx4 v[140:143], v228, s[52:53] sc1
	global_load_dwordx4 v[144:147], v229, s[52:53] sc1
	global_load_dwordx4 v[148:151], v230, s[52:53] sc1
.Lq_noearly:
	v_mov_b32_e32 v152, 0x44800000
	v_add_u32_e32 v208, s8, v195
	v_lshl_add_u32 v155, v181, 1, v208
	v_cndmask_b32_e64 v152, v152, 0, s[4:5]
	v_fma_mixlo_f16 v153, v159, v152, 0
	v_fma_mixhi_f16 v153, v160, v152, 0
	s_cmp_lt_u32 s43, 23
	ds_write_b16 v155, v153
	ds_write_b16_d16_hi v155, v153 offset:8
	s_cbranch_scc1 .LBB1_35
	v_fma_mixlo_f16 v154, v159, v152, -v153 op_sel_hi:[0,0,1]
	v_fma_mixhi_f16 v154, v160, v152, -v153 op_sel:[0,0,1] op_sel_hi:[0,0,1]
	ds_write_b16 v155, v154 offset:8448
	ds_write_b16_d16_hi v155, v154 offset:8456
.LBB1_35:
	v_add_u32_e32 v156, s8, v231
	v_add_u32_e32 v157, s8, v232
	v_add_u32_e32 v158, s8, v233
	s_xor_b64 s[8:9], s[10:11], -1
	s_andn2_b64 vcc, exec, s[8:9]
	s_cbranch_vccnz .LBB1_44
	s_branch .Lq_wait

.LBB1_47:
	s_cmp_eq_u32 s43, 31
	s_cbranch_scc0 .Lpost_nosave
	v_mov_b32_e32 v202, v140
	v_mov_b32_e32 v198, v142
	v_mov_b32_e32 v197, v144
	v_mov_b32_e32 v196, v146
	v_mov_b32_e32 v179, v148
	v_mov_b32_e32 v177, v150
.Lpost_nosave:
	v_fma_mixlo_f16 v153, v140, v152, 0
	v_fma_mixhi_f16 v153, v142, v152, 0
	v_fma_mixlo_f16 v154, v144, v152, 0
	v_fma_mixhi_f16 v154, v146, v152, 0
	v_fma_mixlo_f16 v155, v148, v152, 0
	v_fma_mixhi_f16 v155, v150, v152, 0
	ds_write_b32 v156, v153
	ds_write_b32 v157, v154
	ds_write_b32 v158, v155
	s_andn2_b64 vcc, exec, s[38:39]
	s_cbranch_vccnz .LBB1_53
	v_fma_mixlo_f16 v159, v140, v152, -v153 op_sel_hi:[0,0,1]
	v_fma_mixhi_f16 v159, v142, v152, -v153 op_sel:[0,0,1] op_sel_hi:[0,0,1]
	v_fma_mixlo_f16 v160, v144, v152, -v154 op_sel_hi:[0,0,1]
	v_fma_mixhi_f16 v160, v146, v152, -v154 op_sel:[0,0,1] op_sel_hi:[0,0,1]
	v_fma_mixlo_f16 v161, v148, v152, -v155 op_sel_hi:[0,0,1]
	v_fma_mixhi_f16 v161, v150, v152, -v155 op_sel:[0,0,1] op_sel_hi:[0,0,1]
	ds_write_b32 v156, v159 offset:8448
	ds_write_b32 v157, v160 offset:8448
	ds_write_b32 v158, v161 offset:8448
